# stack2: two-row modulate0, NAT prefetch counted waits, scatter epilogue waits, barrier polls top generation word
# speedup vs baseline: 1.0059x; 1.0059x over previous
.LBB0_256:
	s_or_b64 exec, exec, s[10:11]
	v_cvt_f32_u32_e32 v6, v4
	s_waitcnt vmcnt(0)
	v_readfirstlane_b32 s2, v5
	v_sub_u32_e32 v5, 0, v4
	v_rcp_iflag_f32_e32 v6, v6
	v_add_u32_e32 v7, s2, v3
	v_mul_f32_e32 v6, 0x4f7ffffe, v6
	v_cvt_u32_f32_e32 v6, v6
	v_mul_lo_u32 v3, v5, v6
	v_mul_hi_u32 v3, v6, v3
	v_add_u32_e32 v3, v6, v3
	v_mul_hi_u32 v3, v7, v3
	v_mul_lo_u32 v5, v3, v4
	v_sub_u32_e32 v5, v7, v5
	v_add_u32_e32 v6, 1, v3
	v_cmp_ge_u32_e32 vcc, v5, v4
	s_nop 1
	v_cndmask_b32_e32 v3, v3, v6, vcc
	v_sub_u32_e32 v6, v5, v4
	v_cndmask_b32_e32 v5, v5, v6, vcc
	v_add_u32_e32 v6, 1, v3
	v_cmp_ge_u32_e32 vcc, v5, v4
	v_add_u32_e32 v5, 1, v7
	s_nop 0
	v_cndmask_b32_e32 v3, v3, v6, vcc
	v_mul_lo_u32 v6, v4, v3
	v_add_u32_e32 v4, v6, v4
	v_cmp_ne_u32_e32 vcc, v5, v4
	s_and_saveexec_b64 s[8:9], vcc
	s_xor_b64 s[8:9], exec, s[8:9]
	s_cbranch_execz .LBB0_270
	s_waitcnt lgkmcnt(0)
	s_lshl_b32 s14, s95, 8
	s_sub_u32 s14, s6, s14
	s_subb_u32 s15, s7, 0
	s_add_u32 s14, s14, 0x3500
	s_addc_u32 s15, s15, 0
	v_mov_b32_e32 v2, 0
	global_load_dword v2, v2, s[14:15] sc1
	s_waitcnt vmcnt(0)
	v_cmp_eq_u32_e32 vcc, v2, v3
	s_and_saveexec_b64 s[10:11], vcc
	s_cbranch_execz .LBB0_269
	s_add_u32 s12, s84, 0x4200
	s_addc_u32 s13, s85, 0
	s_mov_b32 s2, 1
	s_mov_b64 s[16:17], 0
	v_mov_b32_e32 v2, 0
	s_branch .LBB0_260

.LBB0_1860:
	s_or_b64 exec, exec, s[10:11]
	v_cvt_f32_u32_e32 v6, v4
	s_waitcnt vmcnt(0)
	v_readfirstlane_b32 s2, v5
	v_sub_u32_e32 v5, 0, v4
	v_rcp_iflag_f32_e32 v6, v6
	v_add_u32_e32 v7, s2, v3
	v_mul_f32_e32 v6, 0x4f7ffffe, v6
	v_cvt_u32_f32_e32 v6, v6
	v_mul_lo_u32 v3, v5, v6
	v_mul_hi_u32 v3, v6, v3
	v_add_u32_e32 v3, v6, v3
	v_mul_hi_u32 v3, v7, v3
	v_mul_lo_u32 v5, v3, v4
	v_sub_u32_e32 v5, v7, v5
	v_add_u32_e32 v6, 1, v3
	v_cmp_ge_u32_e32 vcc, v5, v4
	s_nop 1
	v_cndmask_b32_e32 v3, v3, v6, vcc
	v_sub_u32_e32 v6, v5, v4
	v_cndmask_b32_e32 v5, v5, v6, vcc
	v_add_u32_e32 v6, 1, v3
	v_cmp_ge_u32_e32 vcc, v5, v4
	v_add_u32_e32 v5, 1, v7
	s_nop 0
	v_cndmask_b32_e32 v3, v3, v6, vcc
	v_mul_lo_u32 v6, v4, v3
	v_add_u32_e32 v4, v6, v4
	v_cmp_ne_u32_e32 vcc, v5, v4
	s_and_saveexec_b64 s[2:3], vcc
	s_xor_b64 s[8:9], exec, s[2:3]
	s_cbranch_execz .LBB0_1874
	s_waitcnt lgkmcnt(0)
	s_lshl_b32 s14, s95, 8
	s_sub_u32 s14, s6, s14
	s_subb_u32 s15, s7, 0
	s_add_u32 s14, s14, 0x3500
	s_addc_u32 s15, s15, 0
	v_mov_b32_e32 v2, 0
	global_load_dword v2, v2, s[14:15] sc1
	s_waitcnt vmcnt(0)
	v_cmp_eq_u32_e32 vcc, v2, v3
	s_and_saveexec_b64 s[10:11], vcc
	s_cbranch_execz .LBB0_1873
	s_add_u32 s12, s84, 0x4200
	s_addc_u32 s13, s85, 0
	s_mov_b32 s2, 1
	s_mov_b64 s[16:17], 0
	v_mov_b32_e32 v2, 0
	s_branch .LBB0_1864

.LBB0_2036:
	s_or_b64 exec, exec, s[8:9]
	v_cvt_f32_u32_e32 v5, v3
	s_waitcnt vmcnt(0)
	v_readfirstlane_b32 s6, v4
	v_sub_u32_e32 v4, 0, v3
	v_rcp_iflag_f32_e32 v5, v5
	v_add_u32_e32 v6, s6, v2
	v_mul_f32_e32 v5, 0x4f7ffffe, v5
	v_cvt_u32_f32_e32 v5, v5
	v_mul_lo_u32 v2, v4, v5
	v_mul_hi_u32 v2, v5, v2
	v_add_u32_e32 v2, v5, v2
	v_mul_hi_u32 v2, v6, v2
	v_mul_lo_u32 v4, v2, v3
	v_sub_u32_e32 v4, v6, v4
	v_add_u32_e32 v5, 1, v2
	v_cmp_ge_u32_e32 vcc, v4, v3
	s_nop 1
	v_cndmask_b32_e32 v2, v2, v5, vcc
	v_sub_u32_e32 v5, v4, v3
	v_cndmask_b32_e32 v4, v4, v5, vcc
	v_add_u32_e32 v5, 1, v2
	v_cmp_ge_u32_e32 vcc, v4, v3
	v_add_u32_e32 v4, 1, v6
	s_nop 0
	v_cndmask_b32_e32 v2, v2, v5, vcc
	v_mul_lo_u32 v5, v3, v2
	v_add_u32_e32 v3, v5, v3
	v_cmp_ne_u32_e32 vcc, v4, v3
	s_and_saveexec_b64 s[6:7], vcc
	s_xor_b64 s[6:7], exec, s[6:7]
	s_cbranch_execz .LBB0_2050
	s_waitcnt lgkmcnt(0)
	s_lshl_b32 s12, s95, 8
	s_sub_u32 s12, s4, s12
	s_subb_u32 s13, s5, 0
	s_add_u32 s12, s12, 0x3500
	s_addc_u32 s13, s13, 0
	v_mov_b32_e32 v1, 0
	global_load_dword v1, v1, s[12:13] sc1
	s_waitcnt vmcnt(0)
	v_cmp_eq_u32_e32 vcc, v1, v2
	s_and_saveexec_b64 s[8:9], vcc
	s_cbranch_execz .LBB0_2049
	s_add_u32 s10, s84, 0x4200
	s_addc_u32 s11, s85, 0
	s_mov_b32 s24, 1
	s_mov_b64 s[14:15], 0
	v_mov_b32_e32 v1, 0
	s_branch .LBB0_2040

.LBB0_2111:
	s_or_b64 exec, exec, s[6:7]
	v_cvt_f32_u32_e32 v4, v2
	s_waitcnt vmcnt(0)
	v_readfirstlane_b32 s4, v3
	v_sub_u32_e32 v3, 0, v2
	v_rcp_iflag_f32_e32 v4, v4
	v_add_u32_e32 v5, s4, v1
	v_mul_f32_e32 v4, 0x4f7ffffe, v4
	v_cvt_u32_f32_e32 v4, v4
	v_mul_lo_u32 v1, v3, v4
	v_mul_hi_u32 v1, v4, v1
	v_add_u32_e32 v1, v4, v1
	v_mul_hi_u32 v1, v5, v1
	v_mul_lo_u32 v3, v1, v2
	v_sub_u32_e32 v3, v5, v3
	v_add_u32_e32 v4, 1, v1
	v_cmp_ge_u32_e32 vcc, v3, v2
	s_nop 1
	v_cndmask_b32_e32 v1, v1, v4, vcc
	v_sub_u32_e32 v4, v3, v2
	v_cndmask_b32_e32 v3, v3, v4, vcc
	v_add_u32_e32 v4, 1, v1
	v_cmp_ge_u32_e32 vcc, v3, v2
	v_add_u32_e32 v3, 1, v5
	s_nop 0
	v_cndmask_b32_e32 v1, v1, v4, vcc
	v_mul_lo_u32 v4, v2, v1
	v_add_u32_e32 v2, v4, v2
	v_cmp_ne_u32_e32 vcc, v3, v2
	s_and_saveexec_b64 s[4:5], vcc
	s_xor_b64 s[4:5], exec, s[4:5]
	s_cbranch_execz .LBB0_2125
	s_waitcnt lgkmcnt(0)
	s_lshl_b32 s10, s95, 8
	s_sub_u32 s10, s2, s10
	s_subb_u32 s11, s3, 0
	s_add_u32 s10, s10, 0x3500
	s_addc_u32 s11, s11, 0
	v_mov_b32_e32 v0, 0
	global_load_dword v0, v0, s[10:11] sc1
	s_waitcnt vmcnt(0)
	v_cmp_eq_u32_e32 vcc, v0, v1
	s_and_saveexec_b64 s[6:7], vcc
	s_cbranch_execz .LBB0_2124
	s_add_u32 s8, s84, 0x4200
	s_addc_u32 s9, s85, 0
	s_mov_b32 s22, 1
	s_mov_b64 s[12:13], 0
	v_mov_b32_e32 v0, 0
	s_branch .LBB0_2115
